# first eight V-fragment reads of the P.V section issued in front of the LDS-DMA block instead of behind it: the DMA issue time covers the LDS latency the first P.V wait used to expose
# baseline (speedup 1.0000x reference)
.LBB0_787:
	ds_read_b128 v[80:83], v134 offset:33792
	ds_read_b128 v[84:87], v134 offset:41984
	ds_read_b128 v[196:199], v135 offset:33792
	ds_read_b128 v[200:203], v135 offset:41984
	s_waitcnt lgkmcnt(2)
	v_mfma_f32_32x32x16_bf16 v[96:111], v[80:83], v[122:125], 0
	v_exp_f32_e32 v204, v72
	v_exp_f32_e32 v205, v73
	v_exp_f32_e32 v206, v74
	v_exp_f32_e32 v207, v75
	v_exp_f32_e32 v208, v76
	v_exp_f32_e32 v209, v77
	v_mfma_f32_32x32x16_bf16 v[80:95], v[84:87], v[122:125], 0
	v_exp_f32_e32 v210, v78
	v_exp_f32_e32 v79, v79
	s_waitcnt lgkmcnt(0)
	v_mfma_f32_32x32x16_bf16 v[96:111], v[196:199], v[126:129], v[96:111]
	v_mfma_f32_32x32x16_bf16 v[80:95], v[200:203], v[126:129], v[80:95]
	ds_read_b128 v[196:199], v136 offset:33792
	ds_read_b128 v[200:203], v136 offset:41984
	s_waitcnt lgkmcnt(0)
	v_mfma_f32_32x32x16_bf16 v[96:111], v[196:199], v[118:121], v[96:111]
	v_mfma_f32_32x32x16_bf16 v[80:95], v[200:203], v[118:121], v[80:95]
	ds_read_b128 v[196:199], v137 offset:33792
	ds_read_b128 v[200:203], v137 offset:41984
	v_exp_f32_e32 v180, v64
	v_add_f32_e32 v64, v161, v159
	v_add_f32_e32 v195, v157, v160
	v_add_f32_e32 v64, v155, v64
	v_add_f32_e32 v195, v158, v195
	v_add_f32_e32 v64, v154, v64
	v_add_f32_e32 v195, v156, v195
	v_add_f32_e32 v64, v151, v64
	v_add_f32_e32 v195, v153, v195
	v_add_f32_e32 v64, v149, v64
	v_add_f32_e32 v195, v152, v195
	v_add_f32_e32 v64, v147, v64
	s_waitcnt lgkmcnt(0)
	v_mfma_f32_32x32x16_bf16 v[96:111], v[196:199], v[114:117], v[96:111]
	v_exp_f32_e32 v197, v65
	v_add_f32_e32 v195, v150, v195
	v_exp_f32_e32 v198, v66
	v_add_f32_e32 v64, v146, v64
	v_exp_f32_e32 v199, v67
	v_add_f32_e32 v195, v148, v195
	v_add_f32_e32 v64, v180, v64
	v_mfma_f32_32x32x16_bf16 v[80:95], v[200:203], v[114:117], v[80:95]
	v_exp_f32_e32 v200, v68
	v_exp_f32_e32 v201, v69
	v_add_f32_e32 v195, v197, v195
	v_exp_f32_e32 v202, v70
	v_add_f32_e32 v64, v198, v64
	v_exp_f32_e32 v203, v71
	v_add_f32_e32 v195, v199, v195
	v_add_f32_e32 v64, v200, v64
	v_add_f32_e32 v195, v201, v195
	v_add_f32_e32 v64, v202, v64
	v_add_f32_e32 v195, v203, v195
	v_add_f32_e32 v64, v204, v64
	v_add_f32_e32 v195, v205, v195
	v_add_f32_e32 v64, v206, v64
	v_add_f32_e32 v195, v207, v195
	v_add_f32_e32 v64, v208, v64
	v_add_f32_e32 v195, v209, v195
	v_add_f32_e32 v64, v210, v64
	v_add_f32_e32 v195, v79, v195
	v_add_f32_e32 v195, v195, v64
	v_cvt_pk_bf16_f32 v64, v159, v161
	v_cvt_pk_bf16_f32 v65, v157, v160
	v_cvt_pk_bf16_f32 v66, v155, v158
	v_cvt_pk_bf16_f32 v67, v154, v156
	v_cvt_pk_bf16_f32 v68, v151, v153
	v_cvt_pk_bf16_f32 v69, v149, v152
	v_cvt_pk_bf16_f32 v70, v147, v150
	v_cvt_pk_bf16_f32 v71, v146, v148
	v_cvt_pk_bf16_f32 v72, v180, v197
	v_cvt_pk_bf16_f32 v73, v198, v199
	v_cvt_pk_bf16_f32 v74, v200, v201
	v_cvt_pk_bf16_f32 v75, v202, v203
	v_cvt_pk_bf16_f32 v76, v204, v205
	v_cvt_pk_bf16_f32 v77, v206, v207
	v_cvt_pk_bf16_f32 v78, v208, v209
	v_cvt_pk_bf16_f32 v79, v210, v79
	ds_read_b64_tr_b16 v[198:199], v192 offset:1024
	ds_read_b64_tr_b16 v[200:201], v192 offset:3072
	ds_read_b64_tr_b16 v[202:203], v192 offset:5120
	ds_read_b64_tr_b16 v[204:205], v192 offset:7168
	ds_read_b64_tr_b16 v[206:207], v192 offset:9216
	ds_read_b64_tr_b16 v[208:209], v192 offset:11264
	ds_read_b64_tr_b16 v[222:223], v192 offset:13312
	ds_read_b64_tr_b16 v[224:225], v192 offset:15360
	s_add_i32 m0, s84, 0x8400
	s_add_u32 s66, s78, s65
	s_addc_u32 s67, s79, 0
	global_load_lds_dwordx4 v185, s[66:67]
	s_add_i32 m0, s84, 0xa400
	s_add_i32 s64, s65, 0x60000
	global_load_lds_dwordx4 v184, s[66:67]
	s_add_i32 m0, s84, 0xc400
	s_add_u32 s70, s80, s64
	s_addc_u32 s71, s81, 0
	global_load_lds_dwordx4 v183, s[70:71]
	s_add_i32 m0, s84, 0xe400
	s_mov_b32 s65, s64
	global_load_lds_dwordx4 v182, s[70:71]
	s_waitcnt lgkmcnt(0)
	v_mfma_f32_32x32x16_bf16 v[0:15], v[64:67], v[198:201], v[0:15]
	ds_read_b64_tr_b16 v[198:199], v192 offset:1536
	ds_read_b64_tr_b16 v[200:201], v192 offset:3584
	ds_read_b64_tr_b16 v[138:139], v192 offset:9728
	ds_read_b64_tr_b16 v[140:141], v192 offset:11776
	v_mfma_f32_32x32x16_bf16 v[0:15], v[68:71], v[202:205], v[0:15]
	ds_read_b64_tr_b16 v[202:203], v192 offset:5632
	ds_read_b64_tr_b16 v[204:205], v192 offset:7680
	ds_read_b64_tr_b16 v[142:143], v192 offset:13824
	ds_read_b64_tr_b16 v[144:145], v192 offset:15872
	v_mfma_f32_32x32x16_bf16 v[0:15], v[72:75], v[206:209], v[0:15]
	v_mfma_f32_32x32x16_bf16 v[0:15], v[76:79], v[222:225], v[0:15]
	s_waitcnt lgkmcnt(0)
	v_mfma_f32_32x32x16_bf16 v[48:63], v[64:67], v[198:201], v[48:63]
	ds_read_b64_tr_b16 v[198:199], v192 offset:2048
	ds_read_b64_tr_b16 v[200:201], v192 offset:4096
	ds_read_b64_tr_b16 v[206:207], v192 offset:10240
	ds_read_b64_tr_b16 v[208:209], v192 offset:12288
	v_mfma_f32_32x32x16_bf16 v[48:63], v[68:71], v[202:205], v[48:63]
	ds_read_b64_tr_b16 v[202:203], v192 offset:6144
	ds_read_b64_tr_b16 v[204:205], v192 offset:8192
	ds_read_b64_tr_b16 v[222:223], v192 offset:14336
	ds_read_b64_tr_b16 v[224:225], v192 offset:16384
	v_mfma_f32_32x32x16_bf16 v[48:63], v[72:75], v[138:141], v[48:63]
	v_mfma_f32_32x32x16_bf16 v[48:63], v[76:79], v[142:145], v[48:63]
	s_waitcnt lgkmcnt(0)
	v_mfma_f32_32x32x16_bf16 v[32:47], v[64:67], v[198:201], v[32:47]
	ds_read_b64_tr_b16 v[198:199], v192 offset:2560
	ds_read_b64_tr_b16 v[200:201], v192 offset:4608
	ds_read_b64_tr_b16 v[138:139], v192 offset:10752
	ds_read_b64_tr_b16 v[140:141], v192 offset:12800
	v_mfma_f32_32x32x16_bf16 v[32:47], v[68:71], v[202:205], v[32:47]
	ds_read_b64_tr_b16 v[202:203], v192 offset:6656
	ds_read_b64_tr_b16 v[204:205], v192 offset:8704
	ds_read_b64_tr_b16 v[142:143], v192 offset:14848
	ds_read_b64_tr_b16 v[144:145], v192 offset:16896
	v_mfma_f32_32x32x16_bf16 v[32:47], v[72:75], v[206:209], v[32:47]
	v_mfma_f32_32x32x16_bf16 v[32:47], v[76:79], v[222:225], v[32:47]
	s_waitcnt lgkmcnt(0)
	v_mfma_f32_32x32x16_bf16 v[16:31], v[64:67], v[198:201], v[16:31]
	v_max_f32_e32 v64, v96, v97
	v_max3_f32 v65, v80, v81, v82
	v_max3_f32 v64, v64, v98, v99
	v_max3_f32 v65, v65, v83, v84
	v_max3_f32 v64, v64, v100, v101
	v_mfma_f32_32x32x16_bf16 v[16:31], v[68:71], v[202:205], v[16:31]
	v_max3_f32 v65, v65, v85, v86
	v_max3_f32 v64, v64, v102, v103
	v_max3_f32 v65, v65, v87, v88
	v_max3_f32 v64, v64, v104, v105
	v_max3_f32 v65, v65, v89, v90
	v_max3_f32 v64, v64, v106, v107
	v_max3_f32 v65, v65, v91, v92
	v_mfma_f32_32x32x16_bf16 v[16:31], v[72:75], v[138:141], v[16:31]
	v_max3_f32 v64, v64, v108, v109
	v_max3_f32 v65, v65, v93, v94
	v_max3_f32 v64, v64, v110, v111
	v_max3_f32 v64, v64, v65, v95
	v_mov_b32_e32 v198, 1.0
	v_mfma_f32_32x32x16_bf16 v[16:31], v[76:79], v[142:145], v[16:31]
	v_cmp_ge_f32_e64 s[0:1], s56, v64
	s_cmp_eq_u64 s[0:1], exec
	s_cbranch_scc1 .LBB0_792
	s_branch .LBB0_801

.LBB0_792:
	v_exp_f32_e32 v197, v96
	v_exp_f32_e32 v208, v97
	v_exp_f32_e32 v209, v98
	v_exp_f32_e32 v210, v99
	v_exp_f32_e32 v211, v100
	v_exp_f32_e32 v220, v101
	v_exp_f32_e32 v221, v102
	v_exp_f32_e32 v222, v103
	v_exp_f32_e32 v223, v104
	v_exp_f32_e32 v224, v105
	v_exp_f32_e32 v225, v106
	v_exp_f32_e32 v226, v107
	v_exp_f32_e32 v227, v108
	v_exp_f32_e32 v228, v109
	v_exp_f32_e32 v229, v110
	v_exp_f32_e32 v230, v111
	s_waitcnt vmcnt(4) lgkmcnt(0)
	s_barrier
	ds_read_b128 v[64:67], v134 offset:50176
	ds_read_b128 v[68:71], v134 offset:58368
	ds_read_b128 v[200:203], v135 offset:50176
	ds_read_b128 v[204:207], v135 offset:58368
	v_exp_f32_e32 v231, v87
	s_waitcnt lgkmcnt(2)
	v_mfma_f32_32x32x16_bf16 v[96:111], v[64:67], v[122:125], 0
	v_exp_f32_e32 v232, v88
	v_exp_f32_e32 v233, v89
	v_exp_f32_e32 v234, v90
	v_exp_f32_e32 v235, v91
	v_exp_f32_e32 v236, v92
	v_exp_f32_e32 v237, v93
	v_exp_f32_e32 v238, v94
	v_mfma_f32_32x32x16_bf16 v[64:79], v[68:71], v[122:125], 0
	v_exp_f32_e32 v95, v95
	s_waitcnt lgkmcnt(0)
	v_mfma_f32_32x32x16_bf16 v[96:111], v[200:203], v[126:129], v[96:111]
	v_mfma_f32_32x32x16_bf16 v[64:79], v[204:207], v[126:129], v[64:79]
	ds_read_b128 v[200:203], v136 offset:50176
	ds_read_b128 v[204:207], v136 offset:58368
	s_waitcnt lgkmcnt(0)
	v_mfma_f32_32x32x16_bf16 v[96:111], v[200:203], v[118:121], v[96:111]
	v_mfma_f32_32x32x16_bf16 v[64:79], v[204:207], v[118:121], v[64:79]
	ds_read_b128 v[200:203], v137 offset:50176
	ds_read_b128 v[204:207], v137 offset:58368
	s_waitcnt lgkmcnt(0)
	v_mfma_f32_32x32x16_bf16 v[96:111], v[200:203], v[114:117], v[96:111]
	v_exp_f32_e32 v201, v80
	v_add_f32_e32 v80, v208, v197
	v_add_f32_e32 v199, v209, v210
	v_add_f32_e32 v80, v211, v80
	v_add_f32_e32 v199, v220, v199
	v_add_f32_e32 v80, v221, v80
	v_add_f32_e32 v199, v222, v199
	v_add_f32_e32 v80, v223, v80
	v_add_f32_e32 v199, v224, v199
	v_add_f32_e32 v80, v225, v80
	v_add_f32_e32 v199, v226, v199
	v_add_f32_e32 v80, v227, v80
	v_exp_f32_e32 v202, v81
	v_add_f32_e32 v199, v228, v199
	v_exp_f32_e32 v203, v82
	v_add_f32_e32 v80, v229, v80
	v_mfma_f32_32x32x16_bf16 v[64:79], v[204:207], v[114:117], v[64:79]
	v_exp_f32_e32 v204, v83
	v_add_f32_e32 v199, v230, v199
	v_exp_f32_e32 v205, v84
	v_add_f32_e32 v80, v201, v80
	v_exp_f32_e32 v206, v85
	v_add_f32_e32 v199, v202, v199
	v_exp_f32_e32 v207, v86
	v_add_f32_e32 v80, v203, v80
	v_add_f32_e32 v199, v204, v199
	v_add_f32_e32 v80, v205, v80
	v_add_f32_e32 v199, v206, v199
	v_add_f32_e32 v80, v207, v80
	v_add_f32_e32 v199, v231, v199
	v_add_f32_e32 v80, v232, v80
	v_add_f32_e32 v199, v233, v199
	v_add_f32_e32 v80, v234, v80
	v_add_f32_e32 v199, v235, v199
	v_add_f32_e32 v80, v236, v80
	v_add_f32_e32 v199, v237, v199
	v_add_f32_e32 v80, v238, v80
	v_add_f32_e32 v199, v95, v199
	v_add_f32_e32 v199, v199, v80
	v_cvt_pk_bf16_f32 v80, v197, v208
	v_cvt_pk_bf16_f32 v81, v209, v210
	v_cvt_pk_bf16_f32 v82, v211, v220
	v_cvt_pk_bf16_f32 v83, v221, v222
	v_cvt_pk_bf16_f32 v84, v223, v224
	v_cvt_pk_bf16_f32 v85, v225, v226
	v_cvt_pk_bf16_f32 v86, v227, v228
	v_cvt_pk_bf16_f32 v87, v229, v230
	v_cvt_pk_bf16_f32 v88, v201, v202
	v_cvt_pk_bf16_f32 v89, v203, v204
	v_cvt_pk_bf16_f32 v90, v205, v206
	v_cvt_pk_bf16_f32 v91, v207, v231
	v_cvt_pk_bf16_f32 v92, v232, v233
	v_cvt_pk_bf16_f32 v93, v234, v235
	v_cvt_pk_bf16_f32 v94, v236, v237
	v_cvt_pk_bf16_f32 v95, v238, v95
	ds_read_b64_tr_b16 v[202:203], v192 offset:17408
	ds_read_b64_tr_b16 v[204:205], v192 offset:19456
	ds_read_b64_tr_b16 v[206:207], v192 offset:21504
	ds_read_b64_tr_b16 v[208:209], v192 offset:23552
	ds_read_b64_tr_b16 v[222:223], v192 offset:25600
	ds_read_b64_tr_b16 v[224:225], v192 offset:27648
	ds_read_b64_tr_b16 v[226:227], v192 offset:29696
	ds_read_b64_tr_b16 v[228:229], v192 offset:31744
	s_add_i32 m0, s84, 0x400
	s_add_u32 s66, s78, s65
	s_addc_u32 s67, s79, 0
	global_load_lds_dwordx4 v185, s[66:67]
	s_add_i32 m0, s84, 0x2400
	s_add_i32 s64, s65, 0x60000
	global_load_lds_dwordx4 v184, s[66:67]
	s_cmp_eq_u32 s55, 29
	s_cselect_b32 s64, s89, s64
	s_add_i32 m0, s84, 0x10400
	s_add_u32 s70, s80, s64
	s_addc_u32 s71, s81, 0
	global_load_lds_dwordx4 v183, s[70:71]
	s_add_i32 m0, s84, 0x12400
	s_mov_b32 s65, s64
	global_load_lds_dwordx4 v182, s[70:71]
.LBB0_794:
	s_waitcnt lgkmcnt(0)
	v_mfma_f32_32x32x16_bf16 v[0:15], v[80:83], v[202:205], v[0:15]
	ds_read_b64_tr_b16 v[202:203], v192 offset:17920
	ds_read_b64_tr_b16 v[204:205], v192 offset:19968
	ds_read_b64_tr_b16 v[138:139], v192 offset:26112
	ds_read_b64_tr_b16 v[140:141], v192 offset:28160
	v_mfma_f32_32x32x16_bf16 v[0:15], v[84:87], v[206:209], v[0:15]
	ds_read_b64_tr_b16 v[206:207], v192 offset:22016
	ds_read_b64_tr_b16 v[208:209], v192 offset:24064
	ds_read_b64_tr_b16 v[142:143], v192 offset:30208
	ds_read_b64_tr_b16 v[144:145], v192 offset:32256
	v_mfma_f32_32x32x16_bf16 v[0:15], v[88:91], v[222:225], v[0:15]
	v_mfma_f32_32x32x16_bf16 v[0:15], v[92:95], v[226:229], v[0:15]
	s_waitcnt lgkmcnt(0)
	v_mfma_f32_32x32x16_bf16 v[48:63], v[80:83], v[202:205], v[48:63]
	ds_read_b64_tr_b16 v[202:203], v192 offset:18432
	ds_read_b64_tr_b16 v[204:205], v192 offset:20480
	ds_read_b64_tr_b16 v[222:223], v192 offset:26624
	ds_read_b64_tr_b16 v[224:225], v192 offset:28672
	v_mfma_f32_32x32x16_bf16 v[48:63], v[84:87], v[206:209], v[48:63]
	ds_read_b64_tr_b16 v[206:207], v192 offset:22528
	ds_read_b64_tr_b16 v[208:209], v192 offset:24576
	ds_read_b64_tr_b16 v[226:227], v192 offset:30720
	ds_read_b64_tr_b16 v[228:229], v192 offset:32768
	v_mfma_f32_32x32x16_bf16 v[48:63], v[88:91], v[138:141], v[48:63]
	v_mfma_f32_32x32x16_bf16 v[48:63], v[92:95], v[142:145], v[48:63]
	s_waitcnt lgkmcnt(0)
	v_mfma_f32_32x32x16_bf16 v[32:47], v[80:83], v[202:205], v[32:47]
	ds_read_b64_tr_b16 v[202:203], v192 offset:18944
	ds_read_b64_tr_b16 v[204:205], v192 offset:20992
	ds_read_b64_tr_b16 v[138:139], v192 offset:27136
	ds_read_b64_tr_b16 v[140:141], v192 offset:29184
	v_mfma_f32_32x32x16_bf16 v[32:47], v[84:87], v[206:209], v[32:47]
	ds_read_b64_tr_b16 v[206:207], v192 offset:23040
	ds_read_b64_tr_b16 v[208:209], v192 offset:25088
	ds_read_b64_tr_b16 v[142:143], v192 offset:31232
	ds_read_b64_tr_b16 v[144:145], v192 offset:33280
	v_mfma_f32_32x32x16_bf16 v[32:47], v[88:91], v[222:225], v[32:47]
	v_mfma_f32_32x32x16_bf16 v[32:47], v[92:95], v[226:229], v[32:47]
	s_waitcnt lgkmcnt(0)
	v_mfma_f32_32x32x16_bf16 v[16:31], v[80:83], v[202:205], v[16:31]
	v_max_f32_e32 v80, v96, v97
	v_max3_f32 v81, v64, v65, v66
	v_max3_f32 v80, v80, v98, v99
	v_max3_f32 v81, v81, v67, v68
	v_max3_f32 v80, v80, v100, v101
	v_mfma_f32_32x32x16_bf16 v[16:31], v[84:87], v[206:209], v[16:31]
	v_max3_f32 v81, v81, v69, v70
	v_max3_f32 v80, v80, v102, v103
	v_max3_f32 v81, v81, v71, v72
	v_max3_f32 v80, v80, v104, v105
	v_max3_f32 v81, v81, v73, v74
	v_max3_f32 v80, v80, v106, v107
	v_max3_f32 v81, v81, v75, v76
	v_mfma_f32_32x32x16_bf16 v[16:31], v[88:91], v[138:141], v[16:31]
	v_max3_f32 v80, v80, v108, v109
	v_max3_f32 v81, v81, v77, v78
	v_max3_f32 v80, v80, v110, v111
	v_max3_f32 v80, v80, v81, v79
	v_mov_b32_e32 v197, 1.0
	v_mfma_f32_32x32x16_bf16 v[16:31], v[92:95], v[142:145], v[16:31]
	v_cmp_ge_f32_e64 s[0:1], s56, v80
	s_cmp_eq_u64 s[0:1], exec
	s_cbranch_scc1 .LBB0_799
	s_branch .LBB0_802

.LBB0_799:
	v_exp_f32_e32 v159, v96
	v_exp_f32_e32 v161, v97
	v_exp_f32_e32 v157, v98
	v_exp_f32_e32 v160, v99
	v_exp_f32_e32 v155, v100
	v_exp_f32_e32 v158, v101
	v_exp_f32_e32 v154, v102
	v_exp_f32_e32 v156, v103
	v_exp_f32_e32 v151, v104
	v_exp_f32_e32 v153, v105
	v_exp_f32_e32 v149, v106
	v_exp_f32_e32 v152, v107
	v_exp_f32_e32 v147, v108
	v_exp_f32_e32 v150, v109
	v_exp_f32_e32 v146, v110
	v_exp_f32_e32 v148, v111
	v_fma_f32 v80, v193, v179, v195
	v_fma_f32 v179, v80, v198, v199
	s_cmp_gt_u32 s55, 32
	s_waitcnt vmcnt(4) lgkmcnt(0)
	s_barrier
	s_cbranch_scc1 .LBB0_803
	s_add_i32 s55, s55, 2
	v_mov_b32_e32 v193, v197
	ds_read_b128 v[80:83], v130 offset:50176
	ds_read_b128 v[84:87], v130 offset:58368
	ds_read_b128 v[196:199], v131 offset:50176
	ds_read_b128 v[200:203], v131 offset:58368
	s_waitcnt lgkmcnt(2)
	v_mfma_f32_32x32x16_bf16 v[96:111], v[80:83], v[122:125], 0
	v_exp_f32_e32 v204, v72
	v_exp_f32_e32 v205, v73
	v_exp_f32_e32 v206, v74
	v_exp_f32_e32 v207, v75
	v_exp_f32_e32 v208, v76
	v_exp_f32_e32 v209, v77
	v_mfma_f32_32x32x16_bf16 v[80:95], v[84:87], v[122:125], 0
	v_exp_f32_e32 v210, v78
	v_exp_f32_e32 v79, v79
	s_waitcnt lgkmcnt(0)
	v_mfma_f32_32x32x16_bf16 v[96:111], v[196:199], v[126:129], v[96:111]
	v_mfma_f32_32x32x16_bf16 v[80:95], v[200:203], v[126:129], v[80:95]
	ds_read_b128 v[196:199], v132 offset:50176
	ds_read_b128 v[200:203], v132 offset:58368
	s_waitcnt lgkmcnt(0)
	v_mfma_f32_32x32x16_bf16 v[96:111], v[196:199], v[118:121], v[96:111]
	v_mfma_f32_32x32x16_bf16 v[80:95], v[200:203], v[118:121], v[80:95]
	ds_read_b128 v[196:199], v133 offset:50176
	ds_read_b128 v[200:203], v133 offset:58368
	v_exp_f32_e32 v180, v64
	v_add_f32_e32 v64, v161, v159
	v_add_f32_e32 v195, v157, v160
	v_add_f32_e32 v64, v155, v64
	v_add_f32_e32 v195, v158, v195
	v_add_f32_e32 v64, v154, v64
	v_add_f32_e32 v195, v156, v195
	v_add_f32_e32 v64, v151, v64
	v_add_f32_e32 v195, v153, v195
	v_add_f32_e32 v64, v149, v64
	v_add_f32_e32 v195, v152, v195
	v_add_f32_e32 v64, v147, v64
	s_waitcnt lgkmcnt(0)
	v_mfma_f32_32x32x16_bf16 v[96:111], v[196:199], v[114:117], v[96:111]
	v_exp_f32_e32 v197, v65
	v_add_f32_e32 v195, v150, v195
	v_exp_f32_e32 v198, v66
	v_add_f32_e32 v64, v146, v64
	v_exp_f32_e32 v199, v67
	v_add_f32_e32 v195, v148, v195
	v_add_f32_e32 v64, v180, v64
	v_mfma_f32_32x32x16_bf16 v[80:95], v[200:203], v[114:117], v[80:95]
	v_exp_f32_e32 v200, v68
	v_exp_f32_e32 v201, v69
	v_add_f32_e32 v195, v197, v195
	v_exp_f32_e32 v202, v70
	v_add_f32_e32 v64, v198, v64
	v_exp_f32_e32 v203, v71
	v_add_f32_e32 v195, v199, v195
	v_add_f32_e32 v64, v200, v64
	v_add_f32_e32 v195, v201, v195
	v_add_f32_e32 v64, v202, v64
	v_add_f32_e32 v195, v203, v195
	v_add_f32_e32 v64, v204, v64
	v_add_f32_e32 v195, v205, v195
	v_add_f32_e32 v64, v206, v64
	v_add_f32_e32 v195, v207, v195
	v_add_f32_e32 v64, v208, v64
	v_add_f32_e32 v195, v209, v195
	v_add_f32_e32 v64, v210, v64
	v_add_f32_e32 v195, v79, v195
	v_add_f32_e32 v195, v195, v64
	v_cvt_pk_bf16_f32 v64, v159, v161
	v_cvt_pk_bf16_f32 v65, v157, v160
	v_cvt_pk_bf16_f32 v66, v155, v158
	v_cvt_pk_bf16_f32 v67, v154, v156
	v_cvt_pk_bf16_f32 v68, v151, v153
	v_cvt_pk_bf16_f32 v69, v149, v152
	v_cvt_pk_bf16_f32 v70, v147, v150
	v_cvt_pk_bf16_f32 v71, v146, v148
	v_cvt_pk_bf16_f32 v72, v180, v197
	v_cvt_pk_bf16_f32 v73, v198, v199
	v_cvt_pk_bf16_f32 v74, v200, v201
	v_cvt_pk_bf16_f32 v75, v202, v203
	v_cvt_pk_bf16_f32 v76, v204, v205
	v_cvt_pk_bf16_f32 v77, v206, v207
	v_cvt_pk_bf16_f32 v78, v208, v209
	v_cvt_pk_bf16_f32 v79, v210, v79
	ds_read_b64_tr_b16 v[198:199], v192 offset:33792
	ds_read_b64_tr_b16 v[200:201], v192 offset:35840
	ds_read_b64_tr_b16 v[202:203], v192 offset:37888
	ds_read_b64_tr_b16 v[204:205], v192 offset:39936
	ds_read_b64_tr_b16 v[206:207], v192 offset:41984
	ds_read_b64_tr_b16 v[208:209], v192 offset:44032
	ds_read_b64_tr_b16 v[222:223], v192 offset:46080
	ds_read_b64_tr_b16 v[224:225], v192 offset:48128
	s_add_i32 m0, s84, 0x4400
	s_add_u32 s66, s78, s65
	s_addc_u32 s67, s79, 0
	global_load_lds_dwordx4 v185, s[66:67]
	s_add_i32 m0, s84, 0x6400
	s_add_i32 s64, s65, 0x60000
	global_load_lds_dwordx4 v184, s[66:67]
	s_add_i32 m0, s84, 0x14400
	s_add_u32 s70, s80, s64
	s_addc_u32 s71, s81, 0
	global_load_lds_dwordx4 v183, s[70:71]
	s_add_i32 m0, s84, 0x16400
	s_mov_b32 s65, s64
	global_load_lds_dwordx4 v182, s[70:71]
	s_waitcnt lgkmcnt(0)
	v_mfma_f32_32x32x16_bf16 v[0:15], v[64:67], v[198:201], v[0:15]
	ds_read_b64_tr_b16 v[198:199], v192 offset:34304
	ds_read_b64_tr_b16 v[200:201], v192 offset:36352
	ds_read_b64_tr_b16 v[138:139], v192 offset:42496
	ds_read_b64_tr_b16 v[140:141], v192 offset:44544
	v_mfma_f32_32x32x16_bf16 v[0:15], v[68:71], v[202:205], v[0:15]
	ds_read_b64_tr_b16 v[202:203], v192 offset:38400
	ds_read_b64_tr_b16 v[204:205], v192 offset:40448
	ds_read_b64_tr_b16 v[142:143], v192 offset:46592
	ds_read_b64_tr_b16 v[144:145], v192 offset:48640
	v_mfma_f32_32x32x16_bf16 v[0:15], v[72:75], v[206:209], v[0:15]
	v_mfma_f32_32x32x16_bf16 v[0:15], v[76:79], v[222:225], v[0:15]
	s_waitcnt lgkmcnt(0)
	v_mfma_f32_32x32x16_bf16 v[48:63], v[64:67], v[198:201], v[48:63]
	ds_read_b64_tr_b16 v[198:199], v192 offset:34816
	ds_read_b64_tr_b16 v[200:201], v192 offset:36864
	ds_read_b64_tr_b16 v[206:207], v192 offset:43008
	ds_read_b64_tr_b16 v[208:209], v192 offset:45056
	v_mfma_f32_32x32x16_bf16 v[48:63], v[68:71], v[202:205], v[48:63]
	ds_read_b64_tr_b16 v[202:203], v192 offset:38912
	ds_read_b64_tr_b16 v[204:205], v192 offset:40960
	ds_read_b64_tr_b16 v[222:223], v192 offset:47104
	ds_read_b64_tr_b16 v[224:225], v192 offset:49152
	v_mfma_f32_32x32x16_bf16 v[48:63], v[72:75], v[138:141], v[48:63]
	v_mfma_f32_32x32x16_bf16 v[48:63], v[76:79], v[142:145], v[48:63]
	s_waitcnt lgkmcnt(0)
	v_mfma_f32_32x32x16_bf16 v[32:47], v[64:67], v[198:201], v[32:47]
	ds_read_b64_tr_b16 v[198:199], v192 offset:35328
	ds_read_b64_tr_b16 v[200:201], v192 offset:37376
	ds_read_b64_tr_b16 v[138:139], v192 offset:43520
	ds_read_b64_tr_b16 v[140:141], v192 offset:45568
	v_mfma_f32_32x32x16_bf16 v[32:47], v[68:71], v[202:205], v[32:47]
	ds_read_b64_tr_b16 v[202:203], v192 offset:39424
	ds_read_b64_tr_b16 v[204:205], v192 offset:41472
	ds_read_b64_tr_b16 v[142:143], v192 offset:47616
	ds_read_b64_tr_b16 v[144:145], v192 offset:49664
	v_mfma_f32_32x32x16_bf16 v[32:47], v[72:75], v[206:209], v[32:47]
	v_mfma_f32_32x32x16_bf16 v[32:47], v[76:79], v[222:225], v[32:47]
	s_waitcnt lgkmcnt(0)
	v_mfma_f32_32x32x16_bf16 v[16:31], v[64:67], v[198:201], v[16:31]
	v_max_f32_e32 v64, v96, v97
	v_max3_f32 v65, v80, v81, v82
	v_max3_f32 v64, v64, v98, v99
	v_max3_f32 v65, v65, v83, v84
	v_max3_f32 v64, v64, v100, v101
	v_mfma_f32_32x32x16_bf16 v[16:31], v[68:71], v[202:205], v[16:31]
	v_max3_f32 v65, v65, v85, v86
	v_max3_f32 v64, v64, v102, v103
	v_max3_f32 v65, v65, v87, v88
	v_max3_f32 v64, v64, v104, v105
	v_max3_f32 v65, v65, v89, v90
	v_max3_f32 v64, v64, v106, v107
	v_max3_f32 v65, v65, v91, v92
	v_mfma_f32_32x32x16_bf16 v[16:31], v[72:75], v[138:141], v[16:31]
	v_max3_f32 v64, v64, v108, v109
	v_max3_f32 v65, v65, v93, v94
	v_max3_f32 v64, v64, v110, v111
	v_max3_f32 v64, v64, v65, v95
	v_mov_b32_e32 v198, 1.0
	v_mfma_f32_32x32x16_bf16 v[16:31], v[76:79], v[142:145], v[16:31]
	v_cmp_ge_f32_e64 s[0:1], s56, v64
	s_cmp_eq_u64 s[0:1], exec
	s_cbranch_scc1 .Lc1_792
	s_branch .Lc1_801

.Lc1_792:
	v_exp_f32_e32 v197, v96
	v_exp_f32_e32 v208, v97
	v_exp_f32_e32 v209, v98
	v_exp_f32_e32 v210, v99
	v_exp_f32_e32 v211, v100
	v_exp_f32_e32 v220, v101
	v_exp_f32_e32 v221, v102
	v_exp_f32_e32 v222, v103
	v_exp_f32_e32 v223, v104
	v_exp_f32_e32 v224, v105
	v_exp_f32_e32 v225, v106
	v_exp_f32_e32 v226, v107
	v_exp_f32_e32 v227, v108
	v_exp_f32_e32 v228, v109
	v_exp_f32_e32 v229, v110
	v_exp_f32_e32 v230, v111
	s_waitcnt vmcnt(4) lgkmcnt(0)
	s_barrier
	ds_read_b128 v[64:67], v134 offset:33792
	ds_read_b128 v[68:71], v134 offset:41984
	ds_read_b128 v[200:203], v135 offset:33792
	ds_read_b128 v[204:207], v135 offset:41984
	v_exp_f32_e32 v231, v87
	s_waitcnt lgkmcnt(2)
	v_mfma_f32_32x32x16_bf16 v[96:111], v[64:67], v[122:125], 0
	v_exp_f32_e32 v232, v88
	v_exp_f32_e32 v233, v89
	v_exp_f32_e32 v234, v90
	v_exp_f32_e32 v235, v91
	v_exp_f32_e32 v236, v92
	v_exp_f32_e32 v237, v93
	v_exp_f32_e32 v238, v94
	v_mfma_f32_32x32x16_bf16 v[64:79], v[68:71], v[122:125], 0
	v_exp_f32_e32 v95, v95
	s_waitcnt lgkmcnt(0)
	v_mfma_f32_32x32x16_bf16 v[96:111], v[200:203], v[126:129], v[96:111]
	v_mfma_f32_32x32x16_bf16 v[64:79], v[204:207], v[126:129], v[64:79]
	ds_read_b128 v[200:203], v136 offset:33792
	ds_read_b128 v[204:207], v136 offset:41984
	s_waitcnt lgkmcnt(0)
	v_mfma_f32_32x32x16_bf16 v[96:111], v[200:203], v[118:121], v[96:111]
	v_mfma_f32_32x32x16_bf16 v[64:79], v[204:207], v[118:121], v[64:79]
	ds_read_b128 v[200:203], v137 offset:33792
	ds_read_b128 v[204:207], v137 offset:41984
	s_waitcnt lgkmcnt(0)
	v_mfma_f32_32x32x16_bf16 v[96:111], v[200:203], v[114:117], v[96:111]
	v_exp_f32_e32 v201, v80
	v_add_f32_e32 v80, v208, v197
	v_add_f32_e32 v199, v209, v210
	v_add_f32_e32 v80, v211, v80
	v_add_f32_e32 v199, v220, v199
	v_add_f32_e32 v80, v221, v80
	v_add_f32_e32 v199, v222, v199
	v_add_f32_e32 v80, v223, v80
	v_add_f32_e32 v199, v224, v199
	v_add_f32_e32 v80, v225, v80
	v_add_f32_e32 v199, v226, v199
	v_add_f32_e32 v80, v227, v80
	v_exp_f32_e32 v202, v81
	v_add_f32_e32 v199, v228, v199
	v_exp_f32_e32 v203, v82
	v_add_f32_e32 v80, v229, v80
	v_mfma_f32_32x32x16_bf16 v[64:79], v[204:207], v[114:117], v[64:79]
	v_exp_f32_e32 v204, v83
	v_add_f32_e32 v199, v230, v199
	v_exp_f32_e32 v205, v84
	v_add_f32_e32 v80, v201, v80
	v_exp_f32_e32 v206, v85
	v_add_f32_e32 v199, v202, v199
	v_exp_f32_e32 v207, v86
	v_add_f32_e32 v80, v203, v80
	v_add_f32_e32 v199, v204, v199
	v_add_f32_e32 v80, v205, v80
	v_add_f32_e32 v199, v206, v199
	v_add_f32_e32 v80, v207, v80
	v_add_f32_e32 v199, v231, v199
	v_add_f32_e32 v80, v232, v80
	v_add_f32_e32 v199, v233, v199
	v_add_f32_e32 v80, v234, v80
	v_add_f32_e32 v199, v235, v199
	v_add_f32_e32 v80, v236, v80
	v_add_f32_e32 v199, v237, v199
	v_add_f32_e32 v80, v238, v80
	v_add_f32_e32 v199, v95, v199
	v_add_f32_e32 v199, v199, v80
	v_cvt_pk_bf16_f32 v80, v197, v208
	v_cvt_pk_bf16_f32 v81, v209, v210
	v_cvt_pk_bf16_f32 v82, v211, v220
	v_cvt_pk_bf16_f32 v83, v221, v222
	v_cvt_pk_bf16_f32 v84, v223, v224
	v_cvt_pk_bf16_f32 v85, v225, v226
	v_cvt_pk_bf16_f32 v86, v227, v228
	v_cvt_pk_bf16_f32 v87, v229, v230
	v_cvt_pk_bf16_f32 v88, v201, v202
	v_cvt_pk_bf16_f32 v89, v203, v204
	v_cvt_pk_bf16_f32 v90, v205, v206
	v_cvt_pk_bf16_f32 v91, v207, v231
	v_cvt_pk_bf16_f32 v92, v232, v233
	v_cvt_pk_bf16_f32 v93, v234, v235
	v_cvt_pk_bf16_f32 v94, v236, v237
	v_cvt_pk_bf16_f32 v95, v238, v95
	ds_read_b64_tr_b16 v[202:203], v192 offset:1024
	ds_read_b64_tr_b16 v[204:205], v192 offset:3072
	ds_read_b64_tr_b16 v[206:207], v192 offset:5120
	ds_read_b64_tr_b16 v[208:209], v192 offset:7168
	ds_read_b64_tr_b16 v[222:223], v192 offset:9216
	ds_read_b64_tr_b16 v[224:225], v192 offset:11264
	ds_read_b64_tr_b16 v[226:227], v192 offset:13312
	ds_read_b64_tr_b16 v[228:229], v192 offset:15360
	s_add_i32 m0, s84, 0x8400
	s_add_u32 s66, s78, s65
	s_addc_u32 s67, s79, 0
	global_load_lds_dwordx4 v185, s[66:67]
	s_add_i32 m0, s84, 0xa400
	s_add_i32 s64, s65, 0x60000
	global_load_lds_dwordx4 v184, s[66:67]
	s_cmp_eq_u32 s55, 29
	s_cselect_b32 s64, s89, s64
	s_add_i32 m0, s84, 0xc400
	s_add_u32 s70, s80, s64
	s_addc_u32 s71, s81, 0
	global_load_lds_dwordx4 v183, s[70:71]
	s_add_i32 m0, s84, 0xe400
	s_mov_b32 s65, s64
	global_load_lds_dwordx4 v182, s[70:71]
.Lc1_794:
	s_waitcnt lgkmcnt(0)
	v_mfma_f32_32x32x16_bf16 v[0:15], v[80:83], v[202:205], v[0:15]
	ds_read_b64_tr_b16 v[202:203], v192 offset:1536
	ds_read_b64_tr_b16 v[204:205], v192 offset:3584
	ds_read_b64_tr_b16 v[138:139], v192 offset:9728
	ds_read_b64_tr_b16 v[140:141], v192 offset:11776
	v_mfma_f32_32x32x16_bf16 v[0:15], v[84:87], v[206:209], v[0:15]
	ds_read_b64_tr_b16 v[206:207], v192 offset:5632
	ds_read_b64_tr_b16 v[208:209], v192 offset:7680
	ds_read_b64_tr_b16 v[142:143], v192 offset:13824
	ds_read_b64_tr_b16 v[144:145], v192 offset:15872
	v_mfma_f32_32x32x16_bf16 v[0:15], v[88:91], v[222:225], v[0:15]
	v_mfma_f32_32x32x16_bf16 v[0:15], v[92:95], v[226:229], v[0:15]
	s_waitcnt lgkmcnt(0)
	v_mfma_f32_32x32x16_bf16 v[48:63], v[80:83], v[202:205], v[48:63]
	ds_read_b64_tr_b16 v[202:203], v192 offset:2048
	ds_read_b64_tr_b16 v[204:205], v192 offset:4096
	ds_read_b64_tr_b16 v[222:223], v192 offset:10240
	ds_read_b64_tr_b16 v[224:225], v192 offset:12288
	v_mfma_f32_32x32x16_bf16 v[48:63], v[84:87], v[206:209], v[48:63]
	ds_read_b64_tr_b16 v[206:207], v192 offset:6144
	ds_read_b64_tr_b16 v[208:209], v192 offset:8192
	ds_read_b64_tr_b16 v[226:227], v192 offset:14336
	ds_read_b64_tr_b16 v[228:229], v192 offset:16384
	v_mfma_f32_32x32x16_bf16 v[48:63], v[88:91], v[138:141], v[48:63]
	v_mfma_f32_32x32x16_bf16 v[48:63], v[92:95], v[142:145], v[48:63]
	s_waitcnt lgkmcnt(0)
	v_mfma_f32_32x32x16_bf16 v[32:47], v[80:83], v[202:205], v[32:47]
	ds_read_b64_tr_b16 v[202:203], v192 offset:2560
	ds_read_b64_tr_b16 v[204:205], v192 offset:4608
	ds_read_b64_tr_b16 v[138:139], v192 offset:10752
	ds_read_b64_tr_b16 v[140:141], v192 offset:12800
	v_mfma_f32_32x32x16_bf16 v[32:47], v[84:87], v[206:209], v[32:47]
	ds_read_b64_tr_b16 v[206:207], v192 offset:6656
	ds_read_b64_tr_b16 v[208:209], v192 offset:8704
	ds_read_b64_tr_b16 v[142:143], v192 offset:14848
	ds_read_b64_tr_b16 v[144:145], v192 offset:16896
	v_mfma_f32_32x32x16_bf16 v[32:47], v[88:91], v[222:225], v[32:47]
	v_mfma_f32_32x32x16_bf16 v[32:47], v[92:95], v[226:229], v[32:47]
	s_waitcnt lgkmcnt(0)
	v_mfma_f32_32x32x16_bf16 v[16:31], v[80:83], v[202:205], v[16:31]
	v_max_f32_e32 v80, v96, v97
	v_max3_f32 v81, v64, v65, v66
	v_max3_f32 v80, v80, v98, v99
	v_max3_f32 v81, v81, v67, v68
	v_max3_f32 v80, v80, v100, v101
	v_mfma_f32_32x32x16_bf16 v[16:31], v[84:87], v[206:209], v[16:31]
	v_max3_f32 v81, v81, v69, v70
	v_max3_f32 v80, v80, v102, v103
	v_max3_f32 v81, v81, v71, v72
	v_max3_f32 v80, v80, v104, v105
	v_max3_f32 v81, v81, v73, v74
	v_max3_f32 v80, v80, v106, v107
	v_max3_f32 v81, v81, v75, v76
	v_mfma_f32_32x32x16_bf16 v[16:31], v[88:91], v[138:141], v[16:31]
	v_max3_f32 v80, v80, v108, v109
	v_max3_f32 v81, v81, v77, v78
	v_max3_f32 v80, v80, v110, v111
	v_max3_f32 v80, v80, v81, v79
	v_mov_b32_e32 v197, 1.0
	v_mfma_f32_32x32x16_bf16 v[16:31], v[92:95], v[142:145], v[16:31]
	v_cmp_ge_f32_e64 s[0:1], s56, v80
	s_cmp_eq_u64 s[0:1], exec
	s_cbranch_scc1 .Lc1_799
	s_branch .Lc1_802

.Lc1_799:
	v_exp_f32_e32 v159, v96
	v_exp_f32_e32 v161, v97
	v_exp_f32_e32 v157, v98
	v_exp_f32_e32 v160, v99
	v_exp_f32_e32 v155, v100
	v_exp_f32_e32 v158, v101
	v_exp_f32_e32 v154, v102
	v_exp_f32_e32 v156, v103
	v_exp_f32_e32 v151, v104
	v_exp_f32_e32 v153, v105
	v_exp_f32_e32 v149, v106
	v_exp_f32_e32 v152, v107
	v_exp_f32_e32 v147, v108
	v_exp_f32_e32 v150, v109
	v_exp_f32_e32 v146, v110
	v_exp_f32_e32 v148, v111
	v_fma_f32 v80, v193, v179, v195
	v_fma_f32 v179, v80, v198, v199
	s_cmp_gt_u32 s55, 32
	s_waitcnt vmcnt(4) lgkmcnt(0)
	s_barrier
	s_cbranch_scc1 .LBB0_803
	s_add_i32 s55, s55, 2
	v_mov_b32_e32 v193, v197
	ds_read_b128 v[80:83], v134 offset:50176
	ds_read_b128 v[84:87], v134 offset:58368
	ds_read_b128 v[196:199], v135 offset:50176
	ds_read_b128 v[200:203], v135 offset:58368
	s_waitcnt lgkmcnt(2)
	v_mfma_f32_32x32x16_bf16 v[96:111], v[80:83], v[122:125], 0
	v_exp_f32_e32 v204, v72
	v_exp_f32_e32 v205, v73
	v_exp_f32_e32 v206, v74
	v_exp_f32_e32 v207, v75
	v_exp_f32_e32 v208, v76
	v_exp_f32_e32 v209, v77
	v_mfma_f32_32x32x16_bf16 v[80:95], v[84:87], v[122:125], 0
	v_exp_f32_e32 v210, v78
	v_exp_f32_e32 v79, v79
	s_waitcnt lgkmcnt(0)
	v_mfma_f32_32x32x16_bf16 v[96:111], v[196:199], v[126:129], v[96:111]
	v_mfma_f32_32x32x16_bf16 v[80:95], v[200:203], v[126:129], v[80:95]
	ds_read_b128 v[196:199], v136 offset:50176
	ds_read_b128 v[200:203], v136 offset:58368
	s_waitcnt lgkmcnt(0)
	v_mfma_f32_32x32x16_bf16 v[96:111], v[196:199], v[118:121], v[96:111]
	v_mfma_f32_32x32x16_bf16 v[80:95], v[200:203], v[118:121], v[80:95]
	ds_read_b128 v[196:199], v137 offset:50176
	ds_read_b128 v[200:203], v137 offset:58368
	v_exp_f32_e32 v180, v64
	v_add_f32_e32 v64, v161, v159
	v_add_f32_e32 v195, v157, v160
	v_add_f32_e32 v64, v155, v64
	v_add_f32_e32 v195, v158, v195
	v_add_f32_e32 v64, v154, v64
	v_add_f32_e32 v195, v156, v195
	v_add_f32_e32 v64, v151, v64
	v_add_f32_e32 v195, v153, v195
	v_add_f32_e32 v64, v149, v64
	v_add_f32_e32 v195, v152, v195
	v_add_f32_e32 v64, v147, v64
	s_waitcnt lgkmcnt(0)
	v_mfma_f32_32x32x16_bf16 v[96:111], v[196:199], v[114:117], v[96:111]
	v_exp_f32_e32 v197, v65
	v_add_f32_e32 v195, v150, v195
	v_exp_f32_e32 v198, v66
	v_add_f32_e32 v64, v146, v64
	v_exp_f32_e32 v199, v67
	v_add_f32_e32 v195, v148, v195
	v_add_f32_e32 v64, v180, v64
	v_mfma_f32_32x32x16_bf16 v[80:95], v[200:203], v[114:117], v[80:95]
	v_exp_f32_e32 v200, v68
	v_exp_f32_e32 v201, v69
	v_add_f32_e32 v195, v197, v195
	v_exp_f32_e32 v202, v70
	v_add_f32_e32 v64, v198, v64
	v_exp_f32_e32 v203, v71
	v_add_f32_e32 v195, v199, v195
	v_add_f32_e32 v64, v200, v64
	v_add_f32_e32 v195, v201, v195
	v_add_f32_e32 v64, v202, v64
	v_add_f32_e32 v195, v203, v195
	v_add_f32_e32 v64, v204, v64
	v_add_f32_e32 v195, v205, v195
	v_add_f32_e32 v64, v206, v64
	v_add_f32_e32 v195, v207, v195
	v_add_f32_e32 v64, v208, v64
	v_add_f32_e32 v195, v209, v195
	v_add_f32_e32 v64, v210, v64
	v_add_f32_e32 v195, v79, v195
	v_add_f32_e32 v195, v195, v64
	v_cvt_pk_bf16_f32 v64, v159, v161
	v_cvt_pk_bf16_f32 v65, v157, v160
	v_cvt_pk_bf16_f32 v66, v155, v158
	v_cvt_pk_bf16_f32 v67, v154, v156
	v_cvt_pk_bf16_f32 v68, v151, v153
	v_cvt_pk_bf16_f32 v69, v149, v152
	v_cvt_pk_bf16_f32 v70, v147, v150
	v_cvt_pk_bf16_f32 v71, v146, v148
	v_cvt_pk_bf16_f32 v72, v180, v197
	v_cvt_pk_bf16_f32 v73, v198, v199
	v_cvt_pk_bf16_f32 v74, v200, v201
	v_cvt_pk_bf16_f32 v75, v202, v203
	v_cvt_pk_bf16_f32 v76, v204, v205
	v_cvt_pk_bf16_f32 v77, v206, v207
	v_cvt_pk_bf16_f32 v78, v208, v209
	v_cvt_pk_bf16_f32 v79, v210, v79
	ds_read_b64_tr_b16 v[198:199], v192 offset:17408
	ds_read_b64_tr_b16 v[200:201], v192 offset:19456
	ds_read_b64_tr_b16 v[202:203], v192 offset:21504
	ds_read_b64_tr_b16 v[204:205], v192 offset:23552
	ds_read_b64_tr_b16 v[206:207], v192 offset:25600
	ds_read_b64_tr_b16 v[208:209], v192 offset:27648
	ds_read_b64_tr_b16 v[222:223], v192 offset:29696
	ds_read_b64_tr_b16 v[224:225], v192 offset:31744
	s_add_i32 m0, s84, 0x400
	s_add_u32 s66, s78, s65
	s_addc_u32 s67, s79, 0
	global_load_lds_dwordx4 v185, s[66:67]
	s_add_i32 m0, s84, 0x2400
	s_add_i32 s64, s65, 0x60000
	global_load_lds_dwordx4 v184, s[66:67]
	s_add_i32 m0, s84, 0x10400
	s_add_u32 s70, s80, s64
	s_addc_u32 s71, s81, 0
	global_load_lds_dwordx4 v183, s[70:71]
	s_add_i32 m0, s84, 0x12400
	s_mov_b32 s65, s64
	global_load_lds_dwordx4 v182, s[70:71]
	s_waitcnt lgkmcnt(0)
	v_mfma_f32_32x32x16_bf16 v[0:15], v[64:67], v[198:201], v[0:15]
	ds_read_b64_tr_b16 v[198:199], v192 offset:17920
	ds_read_b64_tr_b16 v[200:201], v192 offset:19968
	ds_read_b64_tr_b16 v[138:139], v192 offset:26112
	ds_read_b64_tr_b16 v[140:141], v192 offset:28160
	v_mfma_f32_32x32x16_bf16 v[0:15], v[68:71], v[202:205], v[0:15]
	ds_read_b64_tr_b16 v[202:203], v192 offset:22016
	ds_read_b64_tr_b16 v[204:205], v192 offset:24064
	ds_read_b64_tr_b16 v[142:143], v192 offset:30208
	ds_read_b64_tr_b16 v[144:145], v192 offset:32256
	v_mfma_f32_32x32x16_bf16 v[0:15], v[72:75], v[206:209], v[0:15]
	v_mfma_f32_32x32x16_bf16 v[0:15], v[76:79], v[222:225], v[0:15]
	s_waitcnt lgkmcnt(0)
	v_mfma_f32_32x32x16_bf16 v[48:63], v[64:67], v[198:201], v[48:63]
	ds_read_b64_tr_b16 v[198:199], v192 offset:18432
	ds_read_b64_tr_b16 v[200:201], v192 offset:20480
	ds_read_b64_tr_b16 v[206:207], v192 offset:26624
	ds_read_b64_tr_b16 v[208:209], v192 offset:28672
	v_mfma_f32_32x32x16_bf16 v[48:63], v[68:71], v[202:205], v[48:63]
	ds_read_b64_tr_b16 v[202:203], v192 offset:22528
	ds_read_b64_tr_b16 v[204:205], v192 offset:24576
	ds_read_b64_tr_b16 v[222:223], v192 offset:30720
	ds_read_b64_tr_b16 v[224:225], v192 offset:32768
	v_mfma_f32_32x32x16_bf16 v[48:63], v[72:75], v[138:141], v[48:63]
	v_mfma_f32_32x32x16_bf16 v[48:63], v[76:79], v[142:145], v[48:63]
	s_waitcnt lgkmcnt(0)
	v_mfma_f32_32x32x16_bf16 v[32:47], v[64:67], v[198:201], v[32:47]
	ds_read_b64_tr_b16 v[198:199], v192 offset:18944
	ds_read_b64_tr_b16 v[200:201], v192 offset:20992
	ds_read_b64_tr_b16 v[138:139], v192 offset:27136
	ds_read_b64_tr_b16 v[140:141], v192 offset:29184
	v_mfma_f32_32x32x16_bf16 v[32:47], v[68:71], v[202:205], v[32:47]
	ds_read_b64_tr_b16 v[202:203], v192 offset:23040
	ds_read_b64_tr_b16 v[204:205], v192 offset:25088
	ds_read_b64_tr_b16 v[142:143], v192 offset:31232
	ds_read_b64_tr_b16 v[144:145], v192 offset:33280
	v_mfma_f32_32x32x16_bf16 v[32:47], v[72:75], v[206:209], v[32:47]
	v_mfma_f32_32x32x16_bf16 v[32:47], v[76:79], v[222:225], v[32:47]
	s_waitcnt lgkmcnt(0)
	v_mfma_f32_32x32x16_bf16 v[16:31], v[64:67], v[198:201], v[16:31]
	v_max_f32_e32 v64, v96, v97
	v_max3_f32 v65, v80, v81, v82
	v_max3_f32 v64, v64, v98, v99
	v_max3_f32 v65, v65, v83, v84
	v_max3_f32 v64, v64, v100, v101
	v_mfma_f32_32x32x16_bf16 v[16:31], v[68:71], v[202:205], v[16:31]
	v_max3_f32 v65, v65, v85, v86
	v_max3_f32 v64, v64, v102, v103
	v_max3_f32 v65, v65, v87, v88
	v_max3_f32 v64, v64, v104, v105
	v_max3_f32 v65, v65, v89, v90
	v_max3_f32 v64, v64, v106, v107
	v_max3_f32 v65, v65, v91, v92
	v_mfma_f32_32x32x16_bf16 v[16:31], v[72:75], v[138:141], v[16:31]
	v_max3_f32 v64, v64, v108, v109
	v_max3_f32 v65, v65, v93, v94
	v_max3_f32 v64, v64, v110, v111
	v_max3_f32 v64, v64, v65, v95
	v_mov_b32_e32 v198, 1.0
	v_mfma_f32_32x32x16_bf16 v[16:31], v[76:79], v[142:145], v[16:31]
	v_cmp_ge_f32_e64 s[0:1], s56, v64
	s_cmp_eq_u64 s[0:1], exec
	s_cbranch_scc1 .Lc2_792
	s_branch .Lc2_801

.Lc2_792:
	v_exp_f32_e32 v197, v96
	v_exp_f32_e32 v208, v97
	v_exp_f32_e32 v209, v98
	v_exp_f32_e32 v210, v99
	v_exp_f32_e32 v211, v100
	v_exp_f32_e32 v220, v101
	v_exp_f32_e32 v221, v102
	v_exp_f32_e32 v222, v103
	v_exp_f32_e32 v223, v104
	v_exp_f32_e32 v224, v105
	v_exp_f32_e32 v225, v106
	v_exp_f32_e32 v226, v107
	v_exp_f32_e32 v227, v108
	v_exp_f32_e32 v228, v109
	v_exp_f32_e32 v229, v110
	v_exp_f32_e32 v230, v111
	s_waitcnt vmcnt(4) lgkmcnt(0)
	s_barrier
	ds_read_b128 v[64:67], v130 offset:50176
	ds_read_b128 v[68:71], v130 offset:58368
	ds_read_b128 v[200:203], v131 offset:50176
	ds_read_b128 v[204:207], v131 offset:58368
	v_exp_f32_e32 v231, v87
	s_waitcnt lgkmcnt(2)
	v_mfma_f32_32x32x16_bf16 v[96:111], v[64:67], v[122:125], 0
	v_exp_f32_e32 v232, v88
	v_exp_f32_e32 v233, v89
	v_exp_f32_e32 v234, v90
	v_exp_f32_e32 v235, v91
	v_exp_f32_e32 v236, v92
	v_exp_f32_e32 v237, v93
	v_exp_f32_e32 v238, v94
	v_mfma_f32_32x32x16_bf16 v[64:79], v[68:71], v[122:125], 0
	v_exp_f32_e32 v95, v95
	s_waitcnt lgkmcnt(0)
	v_mfma_f32_32x32x16_bf16 v[96:111], v[200:203], v[126:129], v[96:111]
	v_mfma_f32_32x32x16_bf16 v[64:79], v[204:207], v[126:129], v[64:79]
	ds_read_b128 v[200:203], v132 offset:50176
	ds_read_b128 v[204:207], v132 offset:58368
	s_waitcnt lgkmcnt(0)
	v_mfma_f32_32x32x16_bf16 v[96:111], v[200:203], v[118:121], v[96:111]
	v_mfma_f32_32x32x16_bf16 v[64:79], v[204:207], v[118:121], v[64:79]
	ds_read_b128 v[200:203], v133 offset:50176
	ds_read_b128 v[204:207], v133 offset:58368
	s_waitcnt lgkmcnt(0)
	v_mfma_f32_32x32x16_bf16 v[96:111], v[200:203], v[114:117], v[96:111]
	v_exp_f32_e32 v201, v80
	v_add_f32_e32 v80, v208, v197
	v_add_f32_e32 v199, v209, v210
	v_add_f32_e32 v80, v211, v80
	v_add_f32_e32 v199, v220, v199
	v_add_f32_e32 v80, v221, v80
	v_add_f32_e32 v199, v222, v199
	v_add_f32_e32 v80, v223, v80
	v_add_f32_e32 v199, v224, v199
	v_add_f32_e32 v80, v225, v80
	v_add_f32_e32 v199, v226, v199
	v_add_f32_e32 v80, v227, v80
	v_exp_f32_e32 v202, v81
	v_add_f32_e32 v199, v228, v199
	v_exp_f32_e32 v203, v82
	v_add_f32_e32 v80, v229, v80
	v_mfma_f32_32x32x16_bf16 v[64:79], v[204:207], v[114:117], v[64:79]
	v_exp_f32_e32 v204, v83
	v_add_f32_e32 v199, v230, v199
	v_exp_f32_e32 v205, v84
	v_add_f32_e32 v80, v201, v80
	v_exp_f32_e32 v206, v85
	v_add_f32_e32 v199, v202, v199
	v_exp_f32_e32 v207, v86
	v_add_f32_e32 v80, v203, v80
	v_add_f32_e32 v199, v204, v199
	v_add_f32_e32 v80, v205, v80
	v_add_f32_e32 v199, v206, v199
	v_add_f32_e32 v80, v207, v80
	v_add_f32_e32 v199, v231, v199
	v_add_f32_e32 v80, v232, v80
	v_add_f32_e32 v199, v233, v199
	v_add_f32_e32 v80, v234, v80
	v_add_f32_e32 v199, v235, v199
	v_add_f32_e32 v80, v236, v80
	v_add_f32_e32 v199, v237, v199
	v_add_f32_e32 v80, v238, v80
	v_add_f32_e32 v199, v95, v199
	v_add_f32_e32 v199, v199, v80
	v_cvt_pk_bf16_f32 v80, v197, v208
	v_cvt_pk_bf16_f32 v81, v209, v210
	v_cvt_pk_bf16_f32 v82, v211, v220
	v_cvt_pk_bf16_f32 v83, v221, v222
	v_cvt_pk_bf16_f32 v84, v223, v224
	v_cvt_pk_bf16_f32 v85, v225, v226
	v_cvt_pk_bf16_f32 v86, v227, v228
	v_cvt_pk_bf16_f32 v87, v229, v230
	v_cvt_pk_bf16_f32 v88, v201, v202
	v_cvt_pk_bf16_f32 v89, v203, v204
	v_cvt_pk_bf16_f32 v90, v205, v206
	v_cvt_pk_bf16_f32 v91, v207, v231
	v_cvt_pk_bf16_f32 v92, v232, v233
	v_cvt_pk_bf16_f32 v93, v234, v235
	v_cvt_pk_bf16_f32 v94, v236, v237
	v_cvt_pk_bf16_f32 v95, v238, v95
	ds_read_b64_tr_b16 v[202:203], v192 offset:33792
	ds_read_b64_tr_b16 v[204:205], v192 offset:35840
	ds_read_b64_tr_b16 v[206:207], v192 offset:37888
	ds_read_b64_tr_b16 v[208:209], v192 offset:39936
	ds_read_b64_tr_b16 v[222:223], v192 offset:41984
	ds_read_b64_tr_b16 v[224:225], v192 offset:44032
	ds_read_b64_tr_b16 v[226:227], v192 offset:46080
	ds_read_b64_tr_b16 v[228:229], v192 offset:48128
	s_add_i32 m0, s84, 0x4400
	s_add_u32 s66, s78, s65
	s_addc_u32 s67, s79, 0
	global_load_lds_dwordx4 v185, s[66:67]
	s_add_i32 m0, s84, 0x6400
	s_add_i32 s64, s65, 0x60000
	global_load_lds_dwordx4 v184, s[66:67]
	s_cmp_eq_u32 s55, 29
	s_cselect_b32 s64, s89, s64
	s_add_i32 m0, s84, 0x14400
	s_add_u32 s70, s80, s64
	s_addc_u32 s71, s81, 0
	global_load_lds_dwordx4 v183, s[70:71]
	s_add_i32 m0, s84, 0x16400
	s_mov_b32 s65, s64
	global_load_lds_dwordx4 v182, s[70:71]
.Lc2_794:
	s_waitcnt lgkmcnt(0)
	v_mfma_f32_32x32x16_bf16 v[0:15], v[80:83], v[202:205], v[0:15]
	ds_read_b64_tr_b16 v[202:203], v192 offset:34304
	ds_read_b64_tr_b16 v[204:205], v192 offset:36352
	ds_read_b64_tr_b16 v[138:139], v192 offset:42496
	ds_read_b64_tr_b16 v[140:141], v192 offset:44544
	v_mfma_f32_32x32x16_bf16 v[0:15], v[84:87], v[206:209], v[0:15]
	ds_read_b64_tr_b16 v[206:207], v192 offset:38400
	ds_read_b64_tr_b16 v[208:209], v192 offset:40448
	ds_read_b64_tr_b16 v[142:143], v192 offset:46592
	ds_read_b64_tr_b16 v[144:145], v192 offset:48640
	v_mfma_f32_32x32x16_bf16 v[0:15], v[88:91], v[222:225], v[0:15]
	v_mfma_f32_32x32x16_bf16 v[0:15], v[92:95], v[226:229], v[0:15]
	s_waitcnt lgkmcnt(0)
	v_mfma_f32_32x32x16_bf16 v[48:63], v[80:83], v[202:205], v[48:63]
	ds_read_b64_tr_b16 v[202:203], v192 offset:34816
	ds_read_b64_tr_b16 v[204:205], v192 offset:36864
	ds_read_b64_tr_b16 v[222:223], v192 offset:43008
	ds_read_b64_tr_b16 v[224:225], v192 offset:45056
	v_mfma_f32_32x32x16_bf16 v[48:63], v[84:87], v[206:209], v[48:63]
	ds_read_b64_tr_b16 v[206:207], v192 offset:38912
	ds_read_b64_tr_b16 v[208:209], v192 offset:40960
	ds_read_b64_tr_b16 v[226:227], v192 offset:47104
	ds_read_b64_tr_b16 v[228:229], v192 offset:49152
	v_mfma_f32_32x32x16_bf16 v[48:63], v[88:91], v[138:141], v[48:63]
	v_mfma_f32_32x32x16_bf16 v[48:63], v[92:95], v[142:145], v[48:63]
	s_waitcnt lgkmcnt(0)
	v_mfma_f32_32x32x16_bf16 v[32:47], v[80:83], v[202:205], v[32:47]
	ds_read_b64_tr_b16 v[202:203], v192 offset:35328
	ds_read_b64_tr_b16 v[204:205], v192 offset:37376
	ds_read_b64_tr_b16 v[138:139], v192 offset:43520
	ds_read_b64_tr_b16 v[140:141], v192 offset:45568
	v_mfma_f32_32x32x16_bf16 v[32:47], v[84:87], v[206:209], v[32:47]
	ds_read_b64_tr_b16 v[206:207], v192 offset:39424
	ds_read_b64_tr_b16 v[208:209], v192 offset:41472
	ds_read_b64_tr_b16 v[142:143], v192 offset:47616
	ds_read_b64_tr_b16 v[144:145], v192 offset:49664
	v_mfma_f32_32x32x16_bf16 v[32:47], v[88:91], v[222:225], v[32:47]
	v_mfma_f32_32x32x16_bf16 v[32:47], v[92:95], v[226:229], v[32:47]
	s_waitcnt lgkmcnt(0)
	v_mfma_f32_32x32x16_bf16 v[16:31], v[80:83], v[202:205], v[16:31]
	v_max_f32_e32 v80, v96, v97
	v_max3_f32 v81, v64, v65, v66
	v_max3_f32 v80, v80, v98, v99
	v_max3_f32 v81, v81, v67, v68
	v_max3_f32 v80, v80, v100, v101
	v_mfma_f32_32x32x16_bf16 v[16:31], v[84:87], v[206:209], v[16:31]
	v_max3_f32 v81, v81, v69, v70
	v_max3_f32 v80, v80, v102, v103
	v_max3_f32 v81, v81, v71, v72
	v_max3_f32 v80, v80, v104, v105
	v_max3_f32 v81, v81, v73, v74
	v_max3_f32 v80, v80, v106, v107
	v_max3_f32 v81, v81, v75, v76
	v_mfma_f32_32x32x16_bf16 v[16:31], v[88:91], v[138:141], v[16:31]
	v_max3_f32 v80, v80, v108, v109
	v_max3_f32 v81, v81, v77, v78
	v_max3_f32 v80, v80, v110, v111
	v_max3_f32 v80, v80, v81, v79
	v_mov_b32_e32 v197, 1.0
	v_mfma_f32_32x32x16_bf16 v[16:31], v[92:95], v[142:145], v[16:31]
	v_cmp_ge_f32_e64 s[0:1], s56, v80
	s_cmp_eq_u64 s[0:1], exec
	s_cbranch_scc1 .Lc2_799
	s_branch .Lc2_802
